# v2 (next-unit As[1][1] staged before epilogue stores, relaxed first-trip waits, spurious unit-start vmcnt(0) removed) + sc1 write-through policy on the w1 epilogue stores
# baseline (speedup 1.0000x reference)
.LBB0_1233:
	v_lshl_add_u32 v148, s59, 10, v146
	ds_read2_b32 v[150:151], v148 offset1:16
	s_lshl_b32 s17, s58, 2
	v_med3_f32 v124, v124, 0, v193
	v_med3_f32 v125, v125, 0, v193
	s_lshl_b32 s16, s44, 7
	s_or_b32 s17, s17, s45
	s_waitcnt lgkmcnt(0)
	v_mul_f32_e32 v150, v150, v150
	v_pk_mul_f32 v[124:125], v[124:125], v[124:125]
	s_add_i32 s16, s17, s16
	v_pk_mul_f32 v[152:153], v[124:125], v[150:151] op_sel_hi:[1,0]
	v_med3_f32 v124, v130, 0, v193
	v_med3_f32 v125, v131, 0, v193
	s_ashr_i32 s17, s16, 31
	v_med3_f32 v128, v128, 0, v193
	v_med3_f32 v129, v129, 0, v193
	v_med3_f32 v126, v126, 0, v193
	v_med3_f32 v127, v127, 0, v193
	v_pk_mul_f32 v[124:125], v[124:125], v[124:125]
	s_lshl_b64 s[16:17], s[16:17], 15
	v_pk_mul_f32 v[128:129], v[128:129], v[128:129]
	v_pk_mul_f32 v[130:131], v[124:125], v[150:151] op_sel_hi:[1,0]
	v_pk_mul_f32 v[124:125], v[126:127], v[126:127]
	v_med3_f32 v116, v116, 0, v193
	v_med3_f32 v117, v117, 0, v193
	v_lshl_add_u64 v[144:145], v[138:139], 0, s[16:17]
	v_pk_mul_f32 v[128:129], v[128:129], v[150:151] op_sel_hi:[1,0]
	v_pk_mul_f32 v[154:155], v[124:125], v[150:151] op_sel_hi:[1,0]
	v_cvt_pk_bf16_f32 v124, v128, v129
	v_cvt_pk_bf16_f32 v125, v130, v131
	v_pk_mul_f32 v[116:117], v[116:117], v[116:117]
	v_cvt_pk_bf16_f32 v126, v152, v153
	v_cvt_pk_bf16_f32 v127, v154, v155
	global_store_dwordx4 v[144:145], v[124:127], off sc1
	v_med3_f32 v120, v120, 0, v193
	v_med3_f32 v121, v121, 0, v193
	v_pk_mul_f32 v[124:125], v[116:117], v[150:151] op_sel_hi:[1,0]
	v_med3_f32 v116, v122, 0, v193
	v_med3_f32 v117, v123, 0, v193
	v_med3_f32 v118, v118, 0, v193
	v_med3_f32 v119, v119, 0, v193
	v_pk_mul_f32 v[116:117], v[116:117], v[116:117]
	v_pk_mul_f32 v[120:121], v[120:121], v[120:121]
	v_pk_mul_f32 v[122:123], v[116:117], v[150:151] op_sel_hi:[1,0]
	v_pk_mul_f32 v[116:117], v[118:119], v[118:119]
	v_pk_mul_f32 v[120:121], v[120:121], v[150:151] op_sel_hi:[1,0]
	v_pk_mul_f32 v[126:127], v[116:117], v[150:151] op_sel_hi:[1,0]
	v_cvt_pk_bf16_f32 v116, v120, v121
	v_med3_f32 v106, v106, 0, v193
	v_med3_f32 v107, v107, 0, v193
	v_cvt_pk_bf16_f32 v117, v122, v123
	v_cvt_pk_bf16_f32 v118, v124, v125
	v_cvt_pk_bf16_f32 v119, v126, v127
	global_store_dwordx4 v[144:145], v[116:119], off offset:64 sc1
	v_pk_mul_f32 v[106:107], v[106:107], v[106:107]
	v_med3_f32 v110, v110, 0, v193
	v_mul_f32_e32 v116, v151, v151
	v_pk_mul_f32 v[118:119], v[106:107], v[116:117] op_sel_hi:[1,0]
	v_med3_f32 v106, v112, 0, v193
	v_med3_f32 v107, v113, 0, v193
	v_med3_f32 v111, v111, 0, v193
	v_med3_f32 v108, v108, 0, v193
	v_med3_f32 v109, v109, 0, v193
	v_pk_mul_f32 v[106:107], v[106:107], v[106:107]
	v_pk_mul_f32 v[110:111], v[110:111], v[110:111]
	v_pk_mul_f32 v[112:113], v[106:107], v[116:117] op_sel_hi:[1,0]
	v_pk_mul_f32 v[106:107], v[108:109], v[108:109]
	v_med3_f32 v98, v98, 0, v193
	v_med3_f32 v99, v99, 0, v193
	v_pk_mul_f32 v[110:111], v[110:111], v[116:117] op_sel_hi:[1,0]
	v_pk_mul_f32 v[120:121], v[106:107], v[116:117] op_sel_hi:[1,0]
	v_cvt_pk_bf16_f32 v106, v110, v111
	v_cvt_pk_bf16_f32 v107, v112, v113
	v_pk_mul_f32 v[98:99], v[98:99], v[98:99]
	v_cvt_pk_bf16_f32 v108, v118, v119
	v_cvt_pk_bf16_f32 v109, v120, v121
	global_store_dwordx4 v[144:145], v[106:109], off offset:2048 sc1
	v_med3_f32 v102, v102, 0, v193
	v_med3_f32 v103, v103, 0, v193
	v_pk_mul_f32 v[106:107], v[98:99], v[116:117] op_sel_hi:[1,0]
	v_med3_f32 v98, v104, 0, v193
	v_med3_f32 v99, v105, 0, v193
	v_pk_mul_f32 v[102:103], v[102:103], v[102:103]
	v_med3_f32 v100, v100, 0, v193
	v_med3_f32 v101, v101, 0, v193
	v_pk_mul_f32 v[98:99], v[98:99], v[98:99]
	v_pk_mul_f32 v[102:103], v[102:103], v[116:117] op_sel_hi:[1,0]
	v_pk_mul_f32 v[104:105], v[98:99], v[116:117] op_sel_hi:[1,0]
	v_pk_mul_f32 v[98:99], v[100:101], v[100:101]
	v_med3_f32 v90, v90, 0, v193
	v_pk_mul_f32 v[108:109], v[98:99], v[116:117] op_sel_hi:[1,0]
	v_cvt_pk_bf16_f32 v98, v102, v103
	ds_read2_b32 v[102:103], v148 offset0:32 offset1:48
	v_med3_f32 v91, v91, 0, v193
	v_cvt_pk_bf16_f32 v99, v104, v105
	v_cvt_pk_bf16_f32 v100, v106, v107
	v_cvt_pk_bf16_f32 v101, v108, v109
	global_store_dwordx4 v[144:145], v[98:101], off offset:2112 sc1
	v_pk_mul_f32 v[90:91], v[90:91], v[90:91]
	v_med3_f32 v94, v94, 0, v193
	s_waitcnt lgkmcnt(0)
	v_mul_f32_e32 v98, v102, v102
	v_med3_f32 v95, v95, 0, v193
	v_pk_mul_f32 v[100:101], v[90:91], v[98:99] op_sel_hi:[1,0]
	v_med3_f32 v90, v96, 0, v193
	v_med3_f32 v91, v97, 0, v193
	v_pk_mul_f32 v[94:95], v[94:95], v[94:95]
	v_med3_f32 v92, v92, 0, v193
	v_med3_f32 v93, v93, 0, v193
	v_pk_mul_f32 v[90:91], v[90:91], v[90:91]
	v_pk_mul_f32 v[94:95], v[94:95], v[98:99] op_sel_hi:[1,0]
	v_pk_mul_f32 v[96:97], v[90:91], v[98:99] op_sel_hi:[1,0]
	v_pk_mul_f32 v[90:91], v[92:93], v[92:93]
	v_med3_f32 v82, v82, 0, v193
	v_pk_mul_f32 v[104:105], v[90:91], v[98:99] op_sel_hi:[1,0]
	v_cvt_pk_bf16_f32 v90, v94, v95
	v_add_co_u32_e32 v94, vcc, s73, v144
	v_med3_f32 v83, v83, 0, v193
	v_cvt_pk_bf16_f32 v91, v96, v97
	s_nop 0
	v_addc_co_u32_e32 v95, vcc, 0, v145, vcc
	v_pk_mul_f32 v[82:83], v[82:83], v[82:83]
	v_cvt_pk_bf16_f32 v92, v100, v101
	v_cvt_pk_bf16_f32 v93, v104, v105
	global_store_dwordx4 v[94:95], v[90:93], off sc1
	v_med3_f32 v86, v86, 0, v193
	v_med3_f32 v87, v87, 0, v193
	v_pk_mul_f32 v[90:91], v[82:83], v[98:99] op_sel_hi:[1,0]
	v_med3_f32 v82, v88, 0, v193
	v_med3_f32 v83, v89, 0, v193
	v_med3_f32 v84, v84, 0, v193
	v_med3_f32 v85, v85, 0, v193
	v_pk_mul_f32 v[82:83], v[82:83], v[82:83]
	v_pk_mul_f32 v[86:87], v[86:87], v[86:87]
	v_pk_mul_f32 v[88:89], v[82:83], v[98:99] op_sel_hi:[1,0]
	v_pk_mul_f32 v[82:83], v[84:85], v[84:85]
	v_pk_mul_f32 v[86:87], v[86:87], v[98:99] op_sel_hi:[1,0]
	v_pk_mul_f32 v[92:93], v[82:83], v[98:99] op_sel_hi:[1,0]
	v_cvt_pk_bf16_f32 v82, v86, v87
	v_med3_f32 v74, v74, 0, v193
	v_med3_f32 v75, v75, 0, v193
	v_cvt_pk_bf16_f32 v83, v88, v89
	v_cvt_pk_bf16_f32 v84, v90, v91
	v_cvt_pk_bf16_f32 v85, v92, v93
	global_store_dwordx4 v[94:95], v[82:85], off offset:64 sc1
	v_pk_mul_f32 v[74:75], v[74:75], v[74:75]
	v_med3_f32 v78, v78, 0, v193
	v_mul_f32_e32 v82, v103, v103
	v_pk_mul_f32 v[84:85], v[74:75], v[82:83] op_sel_hi:[1,0]
	v_med3_f32 v74, v80, 0, v193
	v_med3_f32 v75, v81, 0, v193
	v_med3_f32 v79, v79, 0, v193
	v_med3_f32 v76, v76, 0, v193
	v_med3_f32 v77, v77, 0, v193
	v_pk_mul_f32 v[74:75], v[74:75], v[74:75]
	v_pk_mul_f32 v[78:79], v[78:79], v[78:79]
	v_pk_mul_f32 v[80:81], v[74:75], v[82:83] op_sel_hi:[1,0]
	v_pk_mul_f32 v[74:75], v[76:77], v[76:77]
	v_med3_f32 v66, v66, 0, v193
	v_med3_f32 v67, v67, 0, v193
	v_pk_mul_f32 v[78:79], v[78:79], v[82:83] op_sel_hi:[1,0]
	v_pk_mul_f32 v[86:87], v[74:75], v[82:83] op_sel_hi:[1,0]
	v_cvt_pk_bf16_f32 v74, v78, v79
	v_cvt_pk_bf16_f32 v75, v80, v81
	v_pk_mul_f32 v[66:67], v[66:67], v[66:67]
	v_cvt_pk_bf16_f32 v76, v84, v85
	v_cvt_pk_bf16_f32 v77, v86, v87
	global_store_dwordx4 v[94:95], v[74:77], off offset:2048 sc1
	v_med3_f32 v70, v70, 0, v193
	v_med3_f32 v71, v71, 0, v193
	v_pk_mul_f32 v[74:75], v[66:67], v[82:83] op_sel_hi:[1,0]
	v_med3_f32 v66, v72, 0, v193
	v_med3_f32 v67, v73, 0, v193
	v_pk_mul_f32 v[70:71], v[70:71], v[70:71]
	v_med3_f32 v68, v68, 0, v193
	v_med3_f32 v69, v69, 0, v193
	v_pk_mul_f32 v[66:67], v[66:67], v[66:67]
	v_pk_mul_f32 v[70:71], v[70:71], v[82:83] op_sel_hi:[1,0]
	v_pk_mul_f32 v[72:73], v[66:67], v[82:83] op_sel_hi:[1,0]
	v_pk_mul_f32 v[66:67], v[68:69], v[68:69]
	v_med3_f32 v64, v64, 0, v193
	v_pk_mul_f32 v[76:77], v[66:67], v[82:83] op_sel_hi:[1,0]
	v_cvt_pk_bf16_f32 v66, v70, v71
	ds_read2_b32 v[70:71], v148 offset0:128 offset1:144
	v_med3_f32 v65, v65, 0, v193
	v_cvt_pk_bf16_f32 v67, v72, v73
	v_cvt_pk_bf16_f32 v68, v74, v75
	v_cvt_pk_bf16_f32 v69, v76, v77
	global_store_dwordx4 v[94:95], v[66:69], off offset:2112 sc1
	v_med3_f32 v60, v60, 0, v193
	v_med3_f32 v61, v61, 0, v193
	s_waitcnt lgkmcnt(0)
	v_mul_f32_e32 v66, v70, v70
	v_pk_mul_f32 v[64:65], v[64:65], v[64:65]
	v_med3_f32 v62, v62, 0, v193
	v_med3_f32 v63, v63, 0, v193
	v_med3_f32 v58, v58, 0, v193
	v_med3_f32 v59, v59, 0, v193
	v_pk_mul_f32 v[64:65], v[64:65], v[66:67] op_sel_hi:[1,0]
	v_pk_mul_f32 v[60:61], v[60:61], v[60:61]
	v_pk_mul_f32 v[62:63], v[62:63], v[62:63]
	v_pk_mul_f32 v[58:59], v[58:59], v[58:59]
	v_pk_mul_f32 v[68:69], v[60:61], v[66:67] op_sel_hi:[1,0]
	v_cvt_pk_bf16_f32 v61, v64, v65
	v_add_co_u32_e32 v64, vcc, s72, v144
	v_pk_mul_f32 v[62:63], v[62:63], v[66:67] op_sel_hi:[1,0]
	v_pk_mul_f32 v[58:59], v[58:59], v[66:67] op_sel_hi:[1,0]
	v_addc_co_u32_e32 v65, vcc, 0, v145, vcc
	v_cvt_pk_bf16_f32 v60, v62, v63
	v_cvt_pk_bf16_f32 v62, v58, v59
	v_add_co_u32_e32 v58, vcc, s31, v144
	v_med3_f32 v50, v50, 0, v193
	v_med3_f32 v51, v51, 0, v193
	v_addc_co_u32_e32 v59, vcc, 0, v145, vcc
	v_pk_mul_f32 v[50:51], v[50:51], v[50:51]
	v_cvt_pk_bf16_f32 v63, v68, v69
	global_store_dwordx4 v[58:59], v[60:63], off offset:-4096 sc1
	v_med3_f32 v54, v54, 0, v193
	v_med3_f32 v55, v55, 0, v193
	v_pk_mul_f32 v[60:61], v[50:51], v[66:67] op_sel_hi:[1,0]
	v_med3_f32 v50, v56, 0, v193
	v_med3_f32 v51, v57, 0, v193
	v_med3_f32 v52, v52, 0, v193
	v_med3_f32 v53, v53, 0, v193
	v_pk_mul_f32 v[50:51], v[50:51], v[50:51]
	v_pk_mul_f32 v[54:55], v[54:55], v[54:55]
	v_pk_mul_f32 v[56:57], v[50:51], v[66:67] op_sel_hi:[1,0]
	v_pk_mul_f32 v[50:51], v[52:53], v[52:53]
	v_pk_mul_f32 v[54:55], v[54:55], v[66:67] op_sel_hi:[1,0]
	v_pk_mul_f32 v[62:63], v[50:51], v[66:67] op_sel_hi:[1,0]
	v_cvt_pk_bf16_f32 v50, v54, v55
	v_med3_f32 v42, v42, 0, v193
	v_med3_f32 v43, v43, 0, v193
	v_cvt_pk_bf16_f32 v51, v56, v57
	v_cvt_pk_bf16_f32 v52, v60, v61
	v_cvt_pk_bf16_f32 v53, v62, v63
	global_store_dwordx4 v[64:65], v[50:53], off offset:64 sc1
	v_pk_mul_f32 v[42:43], v[42:43], v[42:43]
	v_med3_f32 v46, v46, 0, v193
	v_mul_f32_e32 v50, v71, v71
	v_pk_mul_f32 v[52:53], v[42:43], v[50:51] op_sel_hi:[1,0]
	v_med3_f32 v42, v48, 0, v193
	v_med3_f32 v43, v49, 0, v193
	v_med3_f32 v47, v47, 0, v193
	v_med3_f32 v44, v44, 0, v193
	v_med3_f32 v45, v45, 0, v193
	v_pk_mul_f32 v[42:43], v[42:43], v[42:43]
	v_pk_mul_f32 v[46:47], v[46:47], v[46:47]
	v_pk_mul_f32 v[48:49], v[42:43], v[50:51] op_sel_hi:[1,0]
	v_pk_mul_f32 v[42:43], v[44:45], v[44:45]
	v_med3_f32 v34, v34, 0, v193
	v_med3_f32 v35, v35, 0, v193
	v_pk_mul_f32 v[46:47], v[46:47], v[50:51] op_sel_hi:[1,0]
	v_pk_mul_f32 v[54:55], v[42:43], v[50:51] op_sel_hi:[1,0]
	v_cvt_pk_bf16_f32 v42, v46, v47
	v_cvt_pk_bf16_f32 v43, v48, v49
	v_pk_mul_f32 v[34:35], v[34:35], v[34:35]
	v_cvt_pk_bf16_f32 v44, v52, v53
	v_cvt_pk_bf16_f32 v45, v54, v55
	global_store_dwordx4 v[64:65], v[42:45], off offset:2048 sc1
	v_med3_f32 v38, v38, 0, v193
	v_med3_f32 v39, v39, 0, v193
	v_pk_mul_f32 v[42:43], v[34:35], v[50:51] op_sel_hi:[1,0]
	v_med3_f32 v34, v40, 0, v193
	v_med3_f32 v35, v41, 0, v193
	v_pk_mul_f32 v[38:39], v[38:39], v[38:39]
	v_med3_f32 v36, v36, 0, v193
	v_med3_f32 v37, v37, 0, v193
	v_pk_mul_f32 v[34:35], v[34:35], v[34:35]
	v_pk_mul_f32 v[38:39], v[38:39], v[50:51] op_sel_hi:[1,0]
	v_pk_mul_f32 v[40:41], v[34:35], v[50:51] op_sel_hi:[1,0]
	v_pk_mul_f32 v[34:35], v[36:37], v[36:37]
	v_med3_f32 v26, v26, 0, v193
	v_pk_mul_f32 v[44:45], v[34:35], v[50:51] op_sel_hi:[1,0]
	v_cvt_pk_bf16_f32 v34, v38, v39
	ds_read2_b32 v[38:39], v148 offset0:160 offset1:176
	v_med3_f32 v27, v27, 0, v193
	v_cvt_pk_bf16_f32 v35, v40, v41
	v_cvt_pk_bf16_f32 v36, v42, v43
	v_cvt_pk_bf16_f32 v37, v44, v45
	global_store_dwordx4 v[64:65], v[34:37], off offset:2112 sc1
	v_pk_mul_f32 v[26:27], v[26:27], v[26:27]
	v_med3_f32 v30, v30, 0, v193
	s_waitcnt lgkmcnt(0)
	v_mul_f32_e32 v34, v38, v38
	v_pk_mul_f32 v[36:37], v[26:27], v[34:35] op_sel_hi:[1,0]
	v_med3_f32 v26, v32, 0, v193
	v_med3_f32 v27, v33, 0, v193
	v_med3_f32 v31, v31, 0, v193
	v_med3_f32 v28, v28, 0, v193
	v_med3_f32 v29, v29, 0, v193
	v_pk_mul_f32 v[26:27], v[26:27], v[26:27]
	v_pk_mul_f32 v[30:31], v[30:31], v[30:31]
	v_pk_mul_f32 v[32:33], v[26:27], v[34:35] op_sel_hi:[1,0]
	v_pk_mul_f32 v[26:27], v[28:29], v[28:29]
	v_med3_f32 v18, v18, 0, v193
	v_med3_f32 v19, v19, 0, v193
	v_pk_mul_f32 v[30:31], v[30:31], v[34:35] op_sel_hi:[1,0]
	v_pk_mul_f32 v[40:41], v[26:27], v[34:35] op_sel_hi:[1,0]
	v_cvt_pk_bf16_f32 v26, v30, v31
	v_cvt_pk_bf16_f32 v27, v32, v33
	v_pk_mul_f32 v[18:19], v[18:19], v[18:19]
	v_cvt_pk_bf16_f32 v28, v36, v37
	v_cvt_pk_bf16_f32 v29, v40, v41
	global_store_dwordx4 v[58:59], v[26:29], off sc1
	v_med3_f32 v22, v22, 0, v193
	v_med3_f32 v23, v23, 0, v193
	v_pk_mul_f32 v[26:27], v[18:19], v[34:35] op_sel_hi:[1,0]
	v_med3_f32 v18, v24, 0, v193
	v_med3_f32 v19, v25, 0, v193
	v_med3_f32 v20, v20, 0, v193
	v_med3_f32 v21, v21, 0, v193
	v_pk_mul_f32 v[18:19], v[18:19], v[18:19]
	v_pk_mul_f32 v[22:23], v[22:23], v[22:23]
	v_pk_mul_f32 v[24:25], v[18:19], v[34:35] op_sel_hi:[1,0]
	v_pk_mul_f32 v[18:19], v[20:21], v[20:21]
	v_pk_mul_f32 v[22:23], v[22:23], v[34:35] op_sel_hi:[1,0]
	v_pk_mul_f32 v[28:29], v[18:19], v[34:35] op_sel_hi:[1,0]
	v_cvt_pk_bf16_f32 v18, v22, v23
	v_med3_f32 v10, v10, 0, v193
	v_med3_f32 v11, v11, 0, v193
	v_cvt_pk_bf16_f32 v19, v24, v25
	v_cvt_pk_bf16_f32 v20, v26, v27
	v_cvt_pk_bf16_f32 v21, v28, v29
	global_store_dwordx4 v[58:59], v[18:21], off offset:64 sc1
	v_pk_mul_f32 v[10:11], v[10:11], v[10:11]
	v_med3_f32 v14, v14, 0, v193
	v_mul_f32_e32 v18, v39, v39
	v_pk_mul_f32 v[20:21], v[10:11], v[18:19] op_sel_hi:[1,0]
	v_med3_f32 v10, v16, 0, v193
	v_med3_f32 v11, v17, 0, v193
	v_med3_f32 v15, v15, 0, v193
	v_med3_f32 v12, v12, 0, v193
	v_med3_f32 v13, v13, 0, v193
	v_pk_mul_f32 v[10:11], v[10:11], v[10:11]
	v_pk_mul_f32 v[14:15], v[14:15], v[14:15]
	v_pk_mul_f32 v[16:17], v[10:11], v[18:19] op_sel_hi:[1,0]
	v_pk_mul_f32 v[10:11], v[12:13], v[12:13]
	v_med3_f32 v2, v2, 0, v193
	v_med3_f32 v3, v3, 0, v193
	v_pk_mul_f32 v[14:15], v[14:15], v[18:19] op_sel_hi:[1,0]
	v_pk_mul_f32 v[22:23], v[10:11], v[18:19] op_sel_hi:[1,0]
	v_cvt_pk_bf16_f32 v10, v14, v15
	v_cvt_pk_bf16_f32 v11, v16, v17
	v_pk_mul_f32 v[2:3], v[2:3], v[2:3]
	v_cvt_pk_bf16_f32 v12, v20, v21
	v_cvt_pk_bf16_f32 v13, v22, v23
	global_store_dwordx4 v[58:59], v[10:13], off offset:2048 sc1
	v_med3_f32 v6, v6, 0, v193
	v_med3_f32 v7, v7, 0, v193
	v_pk_mul_f32 v[10:11], v[2:3], v[18:19] op_sel_hi:[1,0]
	v_med3_f32 v2, v8, 0, v193
	v_med3_f32 v3, v9, 0, v193
	v_med3_f32 v4, v4, 0, v193
	v_med3_f32 v5, v5, 0, v193
	v_pk_mul_f32 v[2:3], v[2:3], v[2:3]
	v_pk_mul_f32 v[6:7], v[6:7], v[6:7]
	v_pk_mul_f32 v[8:9], v[2:3], v[18:19] op_sel_hi:[1,0]
	v_pk_mul_f32 v[2:3], v[4:5], v[4:5]
	s_andn2_b64 vcc, exec, s[38:39]
	s_mov_b64 s[38:39], -1
	v_pk_mul_f32 v[6:7], v[6:7], v[18:19] op_sel_hi:[1,0]
	v_pk_mul_f32 v[12:13], v[2:3], v[18:19] op_sel_hi:[1,0]
	v_cvt_pk_bf16_f32 v2, v6, v7
	v_cvt_pk_bf16_f32 v3, v8, v9
	v_cvt_pk_bf16_f32 v4, v10, v11
	s_nop 0
	v_cvt_pk_bf16_f32 v5, v12, v13
	global_store_dwordx4 v[58:59], v[2:5], off offset:2112 sc1
	s_cbranch_vccnz .LBB0_1222
	s_andn2_b64 vcc, exec, s[0:1]
	s_cbranch_vccnz .LBB0_1221
	s_barrier
	s_branch .LBB0_1221
